# speedup vs baseline: 1.0311x; 1.0060x over previous
_Z5cvt_wPKfPDF16_S0_S1_iPi:
	s_load_dwordx4 s[4:7], s[0:1], 0x0
	s_load_dwordx2 s[8:9], s[0:1], 0x28
	v_lshrrev_b32_e32 v1, 6, v0
	v_and_b32_e32 v2, 63, v0
	v_readfirstlane_b32 s10, v1
	v_lshlrev_b32_e32 v3, 5, v2
	v_lshlrev_b32_e32 v4, 4, v2
	s_lshl_b32 s11, s2, 2
	s_add_u32 s11, s11, s10
	s_lshl_b32 s12, s11, 13
	s_lshl_b32 s13, s11, 12
	s_waitcnt lgkmcnt(0)
	s_add_u32 s16, s4, s12
	s_addc_u32 s17, s5, 0
	s_add_u32 s14, s6, s13
	s_addc_u32 s15, s7, 0
	s_add_u32 s18, s16, 0x1000
	s_addc_u32 s19, s17, 0
	s_add_u32 s20, s14, 0x1000
	s_addc_u32 s21, s15, 0
	global_load_dwordx4 v[8:11], v3, s[18:19] offset:-4096 nt
	global_load_dwordx4 v[12:15], v3, s[18:19] offset:-4080 nt
	global_load_dwordx4 v[16:19], v3, s[18:19] offset:-2048 nt
	global_load_dwordx4 v[20:23], v3, s[18:19] offset:-2032 nt
	global_load_dwordx4 v[24:27], v3, s[18:19] offset:0 nt
	global_load_dwordx4 v[28:31], v3, s[18:19] offset:16 nt
	global_load_dwordx4 v[32:35], v3, s[18:19] offset:2048 nt
	global_load_dwordx4 v[36:39], v3, s[18:19] offset:2064 nt
	s_waitcnt vmcnt(6)
	v_cvt_pk_f16_f32 v8, v8, v9
	v_cvt_pk_f16_f32 v9, v10, v11
	v_cvt_pk_f16_f32 v10, v12, v13
	v_cvt_pk_f16_f32 v11, v14, v15
	global_store_dwordx4 v4, v[8:11], s[20:21] offset:-4096 sc1
	s_waitcnt vmcnt(5)
	v_cvt_pk_f16_f32 v16, v16, v17
	v_cvt_pk_f16_f32 v17, v18, v19
	v_cvt_pk_f16_f32 v18, v20, v21
	v_cvt_pk_f16_f32 v19, v22, v23
	global_store_dwordx4 v4, v[16:19], s[20:21] offset:-3072 sc1
	s_waitcnt vmcnt(4)
	v_cvt_pk_f16_f32 v24, v24, v25
	v_cvt_pk_f16_f32 v25, v26, v27
	v_cvt_pk_f16_f32 v26, v28, v29
	v_cvt_pk_f16_f32 v27, v30, v31
	global_store_dwordx4 v4, v[24:27], s[20:21] offset:-2048 sc1
	s_waitcnt vmcnt(3)
	v_cvt_pk_f16_f32 v32, v32, v33
	v_cvt_pk_f16_f32 v33, v34, v35
	v_cvt_pk_f16_f32 v34, v36, v37
	v_cvt_pk_f16_f32 v35, v38, v39
	global_store_dwordx4 v4, v[32:35], s[20:21] offset:-1024 sc1
	s_cmp_lg_u32 s2, 0
	s_cbranch_scc1 .Lcw_exit
	v_lshlrev_b32_e32 v1, 2, v0
	v_mov_b32_e32 v2, 0
	global_store_dword v1, v2, s[8:9]

	.amdhsa_kernel _Z5cvt_wPKfPDF16_S0_S1_iPi
		.amdhsa_group_segment_fixed_size 0
		.amdhsa_private_segment_fixed_size 0
		.amdhsa_kernarg_size 304
		.amdhsa_user_sgpr_count 2
		.amdhsa_user_sgpr_dispatch_ptr 0
		.amdhsa_user_sgpr_queue_ptr 0
		.amdhsa_user_sgpr_kernarg_segment_ptr 1
		.amdhsa_user_sgpr_dispatch_id 0
		.amdhsa_user_sgpr_kernarg_preload_length 0
		.amdhsa_user_sgpr_kernarg_preload_offset 0
		.amdhsa_user_sgpr_private_segment_size 0
		.amdhsa_uses_dynamic_stack 0
		.amdhsa_enable_private_segment 0
		.amdhsa_system_sgpr_workgroup_id_x 1
		.amdhsa_system_sgpr_workgroup_id_y 0
		.amdhsa_system_sgpr_workgroup_id_z 0
		.amdhsa_system_sgpr_workgroup_info 0
		.amdhsa_system_vgpr_workitem_id 0
		.amdhsa_next_free_vgpr 40
		.amdhsa_next_free_sgpr 24
		.amdhsa_accum_offset 40
		.amdhsa_reserve_vcc 1
		.amdhsa_float_round_mode_32 0
		.amdhsa_float_round_mode_16_64 0
		.amdhsa_float_denorm_mode_32 3
		.amdhsa_float_denorm_mode_16_64 3
		.amdhsa_dx10_clamp 1
		.amdhsa_ieee_mode 1
		.amdhsa_fp16_overflow 0
		.amdhsa_tg_split 0
		.amdhsa_exception_fp_ieee_invalid_op 0
		.amdhsa_exception_fp_denorm_src 0
		.amdhsa_exception_fp_ieee_div_zero 0
		.amdhsa_exception_fp_ieee_overflow 0
		.amdhsa_exception_fp_ieee_underflow 0
		.amdhsa_exception_fp_ieee_inexact 0
		.amdhsa_exception_int_div_zero 0
	.end_amdhsa_kernel

.LBB1_90:
	s_and_b64 vcc, exec, s[4:5]
	s_cbranch_vccz .LBB1_94
	s_cmpk_ge_u32 s2, 0x300
	s_cbranch_scc1 .LBB1_94
	s_load_dwordx4 s[4:7], s[0:1], 0x38
	v_lshrrev_b32_e32 v1, 6, v0
	v_and_b32_e32 v2, 63, v0
	v_readfirstlane_b32 s10, v1
	v_lshlrev_b32_e32 v3, 5, v2
	v_lshlrev_b32_e32 v4, 4, v2
	s_sub_u32 s11, s2, 0x100
	s_lshl_b32 s11, s11, 3
	s_add_u32 s11, s11, s10
	s_lshl_b32 s12, s11, 14
	s_lshl_b32 s13, s11, 13
	s_waitcnt lgkmcnt(0)
	s_add_u32 s16, s4, s12
	s_addc_u32 s17, s5, 0
	s_add_u32 s14, s6, s13
	s_addc_u32 s15, s7, 0
	s_add_u32 s18, s16, 0x1000
	s_addc_u32 s19, s17, 0
	s_add_u32 s20, s18, 0x2000
	s_addc_u32 s21, s19, 0
	s_add_u32 s22, s14, 0x1000
	s_addc_u32 s23, s15, 0
	global_load_dwordx4 v[8:11], v3, s[18:19] offset:-4096 nt
	global_load_dwordx4 v[12:15], v3, s[18:19] offset:-4080 nt
	global_load_dwordx4 v[16:19], v3, s[18:19] offset:-2048 nt
	global_load_dwordx4 v[20:23], v3, s[18:19] offset:-2032 nt
	global_load_dwordx4 v[24:27], v3, s[18:19] offset:0 nt
	global_load_dwordx4 v[28:31], v3, s[18:19] offset:16 nt
	global_load_dwordx4 v[32:35], v3, s[18:19] offset:2048 nt
	global_load_dwordx4 v[36:39], v3, s[18:19] offset:2064 nt
	global_load_dwordx4 v[40:43], v3, s[20:21] offset:-4096 nt
	global_load_dwordx4 v[44:47], v3, s[20:21] offset:-4080 nt
	global_load_dwordx4 v[48:51], v3, s[20:21] offset:-2048 nt
	global_load_dwordx4 v[52:55], v3, s[20:21] offset:-2032 nt
	global_load_dwordx4 v[56:59], v3, s[20:21] offset:0 nt
	global_load_dwordx4 v[60:63], v3, s[20:21] offset:16 nt
	global_load_dwordx4 v[64:67], v3, s[20:21] offset:2048 nt
	global_load_dwordx4 v[68:71], v3, s[20:21] offset:2064 nt
	s_waitcnt vmcnt(14)
	v_cvt_pk_f16_f32 v8, v8, v9
	v_cvt_pk_f16_f32 v9, v10, v11
	v_cvt_pk_f16_f32 v10, v12, v13
	v_cvt_pk_f16_f32 v11, v14, v15
	global_store_dwordx4 v4, v[8:11], s[22:23] offset:-4096 sc1
	s_waitcnt vmcnt(13)
	v_cvt_pk_f16_f32 v16, v16, v17
	v_cvt_pk_f16_f32 v17, v18, v19
	v_cvt_pk_f16_f32 v18, v20, v21
	v_cvt_pk_f16_f32 v19, v22, v23
	global_store_dwordx4 v4, v[16:19], s[22:23] offset:-3072 sc1
	s_waitcnt vmcnt(12)
	v_cvt_pk_f16_f32 v24, v24, v25
	v_cvt_pk_f16_f32 v25, v26, v27
	v_cvt_pk_f16_f32 v26, v28, v29
	v_cvt_pk_f16_f32 v27, v30, v31
	global_store_dwordx4 v4, v[24:27], s[22:23] offset:-2048 sc1
	s_waitcnt vmcnt(11)
	v_cvt_pk_f16_f32 v32, v32, v33
	v_cvt_pk_f16_f32 v33, v34, v35
	v_cvt_pk_f16_f32 v34, v36, v37
	v_cvt_pk_f16_f32 v35, v38, v39
	global_store_dwordx4 v4, v[32:35], s[22:23] offset:-1024 sc1
	s_waitcnt vmcnt(10)
	v_cvt_pk_f16_f32 v40, v40, v41
	v_cvt_pk_f16_f32 v41, v42, v43
	v_cvt_pk_f16_f32 v42, v44, v45
	v_cvt_pk_f16_f32 v43, v46, v47
	global_store_dwordx4 v4, v[40:43], s[22:23] offset:0 sc1
	s_waitcnt vmcnt(9)
	v_cvt_pk_f16_f32 v48, v48, v49
	v_cvt_pk_f16_f32 v49, v50, v51
	v_cvt_pk_f16_f32 v50, v52, v53
	v_cvt_pk_f16_f32 v51, v54, v55
	global_store_dwordx4 v4, v[48:51], s[22:23] offset:1024 sc1
	s_waitcnt vmcnt(8)
	v_cvt_pk_f16_f32 v56, v56, v57
	v_cvt_pk_f16_f32 v57, v58, v59
	v_cvt_pk_f16_f32 v58, v60, v61
	v_cvt_pk_f16_f32 v59, v62, v63
	global_store_dwordx4 v4, v[56:59], s[22:23] offset:2048 sc1
	s_waitcnt vmcnt(7)
	v_cvt_pk_f16_f32 v64, v64, v65
	v_cvt_pk_f16_f32 v65, v66, v67
	v_cvt_pk_f16_f32 v66, v68, v69
	v_cvt_pk_f16_f32 v67, v70, v71
	global_store_dwordx4 v4, v[64:67], s[22:23] offset:3072 sc1

.Lg2_ntd:
	s_mov_b32 s52, s71
	s_lshl_b32 s57, s51, 8
	s_mul_i32 s54, s52, s50
	s_lshl_b32 s54, s54, 4
	s_add_i32 s55, s53, s54
	s_add_i32 s56, s50, 1
	s_lshr_b32 s56, s56, 1
	s_sub_i32 s22, s50, s56
	s_cmp_eq_u32 s59, 0
	s_cselect_b32 s61, 0, s56
	s_cselect_b32 s62, s56, s22
	s_barrier
	s_mul_i32 s22, s48, 0x400
	s_add_i32 s22, s22, s57
	s_lshl_b32 s23, s60, 7
	s_add_i32 s22, s22, s23
	v_lshl_add_u32 v8, v4, 2, s22
	v_lshlrev_b32_e32 v8, 2, v8
	global_load_dwordx4 v[200:203], v8, s[8:9] offset:0
	global_load_dwordx4 v[204:207], v8, s[8:9] offset:64
	global_load_dwordx4 v[208:211], v8, s[8:9] offset:128
	global_load_dwordx4 v[212:215], v8, s[8:9] offset:192
	global_load_dwordx4 v[216:219], v8, s[8:9] offset:256
	global_load_dwordx4 v[220:223], v8, s[8:9] offset:320
	global_load_dwordx4 v[224:227], v8, s[8:9] offset:384
	global_load_dwordx4 v[228:231], v8, s[8:9] offset:448
	s_lshl_b32 s22, s61, 4
	s_add_i32 s22, s22, s54
	v_add_u32_e32 v241, s22, v3
	s_lshl_b32 s23, s48, 13
	v_add_u32_e32 v8, 0, v241
	v_cmp_gt_u32_e32 vcc, s49, v8
	s_nop 1
	v_cndmask_b32_e32 v8, 0, v8, vcc
	v_add_lshl_u32 v8, v8, s23, 2
	global_load_dword v232, v8, s[16:17]
	v_add_u32_e32 v8, 16, v241
	v_cmp_gt_u32_e32 vcc, s49, v8
	s_nop 1
	v_cndmask_b32_e32 v8, 0, v8, vcc
	v_add_lshl_u32 v8, v8, s23, 2
	global_load_dword v233, v8, s[16:17]
	v_add_u32_e32 v8, 32, v241
	v_cmp_gt_u32_e32 vcc, s49, v8
	s_nop 1
	v_cndmask_b32_e32 v8, 0, v8, vcc
	v_add_lshl_u32 v8, v8, s23, 2
	global_load_dword v234, v8, s[16:17]
	v_add_u32_e32 v8, 48, v241
	v_cmp_gt_u32_e32 vcc, s49, v8
	s_nop 1
	v_cndmask_b32_e32 v8, 0, v8, vcc
	v_add_lshl_u32 v8, v8, s23, 2
	global_load_dword v235, v8, s[16:17]
	v_add_u32_e32 v8, 64, v241
	v_cmp_gt_u32_e32 vcc, s49, v8
	s_nop 1
	v_cndmask_b32_e32 v8, 0, v8, vcc
	v_add_lshl_u32 v8, v8, s23, 2
	global_load_dword v236, v8, s[16:17]
	v_add_u32_e32 v8, s55, v5
	v_mad_u32_u24 v10, v8, s69, v6
	v_add_u32_e32 v11, 0x21000, v10
	v_add_u32_e32 v12, 0x42000, v10
	v_add_u32_e32 v13, 0x63000, v10
	v_add_u32_e32 v14, 0x84000, v10
	s_lshl_b32 s22, s57, 1
	v_add_u32_e32 v20, s22, v7
	v_add_u32_e32 v21, 0x8000, v20
	v_add_u32_e32 v22, 0x10000, v20
	v_add_u32_e32 v23, 0x18000, v20
	v_add_u32_e32 v24, 0x100, v20
	v_add_u32_e32 v25, 0x8100, v20
	v_add_u32_e32 v26, 0x10100, v20
	v_add_u32_e32 v27, 0x18100, v20
	s_lshl_b32 s22, s61, 4
	v_add_u32_e32 v8, s22, v3
	v_lshlrev_b32_e32 v8, 7, v8
	v_lshrrev_b32_e32 v9, 1, v3
	v_xor_b32_e32 v9, v9, v4
	s_and_b32 s22, s61, 1
	v_xor_b32_e32 v9, s22, v9
	v_xor_b32_e32 v56, 0, v9
	v_lshl_add_u32 v30, v56, 4, v8
	v_add_u32_e32 v34, 0xd000, v30
	v_xor_b32_e32 v56, 1, v9
	v_lshl_add_u32 v31, v56, 4, v8
	v_add_u32_e32 v35, 0xd000, v31
	v_xor_b32_e32 v56, 4, v9
	v_lshl_add_u32 v32, v56, 4, v8
	v_add_u32_e32 v36, 0xd000, v32
	v_xor_b32_e32 v56, 5, v9
	v_lshl_add_u32 v33, v56, 4, v8
	v_add_u32_e32 v37, 0xd000, v33
	s_mov_b64 s[64:65], s[4:5]
	s_mul_i32 s22, s48, 0x400000
	s_add_u32 s66, s6, s22
	s_addc_u32 s67, s7, 0
	v_accvgpr_write_b32 a0, 0
	v_accvgpr_write_b32 a1, 0
	v_accvgpr_write_b32 a2, 0
	v_accvgpr_write_b32 a3, 0
	v_accvgpr_write_b32 a4, 0
	v_accvgpr_write_b32 a5, 0
	v_accvgpr_write_b32 a6, 0
	v_accvgpr_write_b32 a7, 0
	v_accvgpr_write_b32 a8, 0
	v_accvgpr_write_b32 a9, 0
	v_accvgpr_write_b32 a10, 0
	v_accvgpr_write_b32 a11, 0
	v_accvgpr_write_b32 a12, 0
	v_accvgpr_write_b32 a13, 0
	v_accvgpr_write_b32 a14, 0
	v_accvgpr_write_b32 a15, 0
	v_accvgpr_write_b32 a16, 0
	v_accvgpr_write_b32 a17, 0
	v_accvgpr_write_b32 a18, 0
	v_accvgpr_write_b32 a19, 0
	v_accvgpr_write_b32 a20, 0
	v_accvgpr_write_b32 a21, 0
	v_accvgpr_write_b32 a22, 0
	v_accvgpr_write_b32 a23, 0
	v_accvgpr_write_b32 a24, 0
	v_accvgpr_write_b32 a25, 0
	v_accvgpr_write_b32 a26, 0
	v_accvgpr_write_b32 a27, 0
	v_accvgpr_write_b32 a28, 0
	v_accvgpr_write_b32 a29, 0
	v_accvgpr_write_b32 a30, 0
	v_accvgpr_write_b32 a31, 0
	v_accvgpr_write_b32 a32, 0
	v_accvgpr_write_b32 a33, 0
	v_accvgpr_write_b32 a34, 0
	v_accvgpr_write_b32 a35, 0
	v_accvgpr_write_b32 a36, 0
	v_accvgpr_write_b32 a37, 0
	v_accvgpr_write_b32 a38, 0
	v_accvgpr_write_b32 a39, 0
	v_accvgpr_write_b32 a40, 0
	v_accvgpr_write_b32 a41, 0
	v_accvgpr_write_b32 a42, 0
	v_accvgpr_write_b32 a43, 0
	v_accvgpr_write_b32 a44, 0
	v_accvgpr_write_b32 a45, 0
	v_accvgpr_write_b32 a46, 0
	v_accvgpr_write_b32 a47, 0
	v_accvgpr_write_b32 a48, 0
	v_accvgpr_write_b32 a49, 0
	v_accvgpr_write_b32 a50, 0
	v_accvgpr_write_b32 a51, 0
	v_accvgpr_write_b32 a52, 0
	v_accvgpr_write_b32 a53, 0
	v_accvgpr_write_b32 a54, 0
	v_accvgpr_write_b32 a55, 0
	v_accvgpr_write_b32 a56, 0
	v_accvgpr_write_b32 a57, 0
	v_accvgpr_write_b32 a58, 0
	v_accvgpr_write_b32 a59, 0
	v_accvgpr_write_b32 a60, 0
	v_accvgpr_write_b32 a61, 0
	v_accvgpr_write_b32 a62, 0
	v_accvgpr_write_b32 a63, 0
	v_accvgpr_write_b32 a64, 0
	v_accvgpr_write_b32 a65, 0
	v_accvgpr_write_b32 a66, 0
	v_accvgpr_write_b32 a67, 0
	v_accvgpr_write_b32 a68, 0
	v_accvgpr_write_b32 a69, 0
	v_accvgpr_write_b32 a70, 0
	v_accvgpr_write_b32 a71, 0
	v_accvgpr_write_b32 a72, 0
	v_accvgpr_write_b32 a73, 0
	v_accvgpr_write_b32 a74, 0
	v_accvgpr_write_b32 a75, 0
	v_accvgpr_write_b32 a76, 0
	v_accvgpr_write_b32 a77, 0
	v_accvgpr_write_b32 a78, 0
	v_accvgpr_write_b32 a79, 0
	v_accvgpr_write_b32 a80, 0
	v_accvgpr_write_b32 a81, 0
	v_accvgpr_write_b32 a82, 0
	v_accvgpr_write_b32 a83, 0
	v_accvgpr_write_b32 a84, 0
	v_accvgpr_write_b32 a85, 0
	v_accvgpr_write_b32 a86, 0
	v_accvgpr_write_b32 a87, 0
	v_accvgpr_write_b32 a88, 0
	v_accvgpr_write_b32 a89, 0
	v_accvgpr_write_b32 a90, 0
	v_accvgpr_write_b32 a91, 0
	v_accvgpr_write_b32 a92, 0
	v_accvgpr_write_b32 a93, 0
	v_accvgpr_write_b32 a94, 0
	v_accvgpr_write_b32 a95, 0
	v_accvgpr_write_b32 a96, 0
	v_accvgpr_write_b32 a97, 0
	v_accvgpr_write_b32 a98, 0
	v_accvgpr_write_b32 a99, 0
	v_accvgpr_write_b32 a100, 0
	v_accvgpr_write_b32 a101, 0
	v_accvgpr_write_b32 a102, 0
	v_accvgpr_write_b32 a103, 0
	v_accvgpr_write_b32 a104, 0
	v_accvgpr_write_b32 a105, 0
	v_accvgpr_write_b32 a106, 0
	v_accvgpr_write_b32 a107, 0
	v_accvgpr_write_b32 a108, 0
	v_accvgpr_write_b32 a109, 0
	v_accvgpr_write_b32 a110, 0
	v_accvgpr_write_b32 a111, 0
	v_accvgpr_write_b32 a112, 0
	v_accvgpr_write_b32 a113, 0
	v_accvgpr_write_b32 a114, 0
	v_accvgpr_write_b32 a115, 0
	v_accvgpr_write_b32 a116, 0
	v_accvgpr_write_b32 a117, 0
	v_accvgpr_write_b32 a118, 0
	v_accvgpr_write_b32 a119, 0
	v_accvgpr_write_b32 a120, 0
	v_accvgpr_write_b32 a121, 0
	v_accvgpr_write_b32 a122, 0
	v_accvgpr_write_b32 a123, 0
	v_accvgpr_write_b32 a124, 0
	v_accvgpr_write_b32 a125, 0
	v_accvgpr_write_b32 a126, 0
	v_accvgpr_write_b32 a127, 0
	v_accvgpr_write_b32 a128, 0
	v_accvgpr_write_b32 a129, 0
	v_accvgpr_write_b32 a130, 0
	v_accvgpr_write_b32 a131, 0
	v_accvgpr_write_b32 a132, 0
	v_accvgpr_write_b32 a133, 0
	v_accvgpr_write_b32 a134, 0
	v_accvgpr_write_b32 a135, 0
	v_accvgpr_write_b32 a136, 0
	v_accvgpr_write_b32 a137, 0
	v_accvgpr_write_b32 a138, 0
	v_accvgpr_write_b32 a139, 0
	v_accvgpr_write_b32 a140, 0
	v_accvgpr_write_b32 a141, 0
	v_accvgpr_write_b32 a142, 0
	v_accvgpr_write_b32 a143, 0
	v_accvgpr_write_b32 a144, 0
	v_accvgpr_write_b32 a145, 0
	v_accvgpr_write_b32 a146, 0
	v_accvgpr_write_b32 a147, 0
	v_accvgpr_write_b32 a148, 0
	v_accvgpr_write_b32 a149, 0
	v_accvgpr_write_b32 a150, 0
	v_accvgpr_write_b32 a151, 0
	v_accvgpr_write_b32 a152, 0
	v_accvgpr_write_b32 a153, 0
	v_accvgpr_write_b32 a154, 0
	v_accvgpr_write_b32 a155, 0
	v_accvgpr_write_b32 a156, 0
	v_accvgpr_write_b32 a157, 0
	v_accvgpr_write_b32 a158, 0
	v_accvgpr_write_b32 a159, 0
	s_mov_b32 s80, 0
	s_mov_b32 s81, 0xd000
	s_mov_b32 s82, 0x1a000
	s_add_u32 s83, s70, s80
	s_add_u32 m0, s83, 0x0
	s_nop 0
	global_load_lds_dwordx4 v10, s[64:65]
	s_add_u32 m0, s83, 0x1000
	s_nop 0
	global_load_lds_dwordx4 v11, s[64:65]
	s_add_u32 m0, s83, 0x2000
	s_nop 0
	global_load_lds_dwordx4 v12, s[64:65]
	s_add_u32 m0, s83, 0x3000
	s_nop 0
	global_load_lds_dwordx4 v13, s[64:65]
	s_add_u32 m0, s83, 0x4000
	s_nop 0
	global_load_lds_dwordx4 v14, s[64:65]
	s_add_u32 m0, s83, 0x5000
	s_nop 0
	global_load_lds_dwordx4 v20, s[66:67]
	s_add_u32 m0, s83, 0x6000
	s_nop 0
	global_load_lds_dwordx4 v21, s[66:67]
	s_add_u32 m0, s83, 0x7000
	s_nop 0
	global_load_lds_dwordx4 v22, s[66:67]
	s_add_u32 m0, s83, 0x8000
	s_nop 0
	global_load_lds_dwordx4 v23, s[66:67]
	s_add_u32 m0, s83, 0x9000
	s_nop 0
	global_load_lds_dwordx4 v24, s[66:67]
	s_add_u32 m0, s83, 0xa000
	s_nop 0
	global_load_lds_dwordx4 v25, s[66:67]
	s_add_u32 m0, s83, 0xb000
	s_nop 0
	global_load_lds_dwordx4 v26, s[66:67]
	s_add_u32 m0, s83, 0xc000
	s_nop 0
	global_load_lds_dwordx4 v27, s[66:67]
	s_add_u32 s64, s64, 0x80
	s_addc_u32 s65, s65, 0
	s_add_u32 s66, s66, 0x20000
	s_addc_u32 s67, s67, 0
	s_add_u32 s83, s70, s81
	s_add_u32 m0, s83, 0x0
	s_nop 0
	global_load_lds_dwordx4 v10, s[64:65]
	s_add_u32 m0, s83, 0x1000
	s_nop 0
	global_load_lds_dwordx4 v11, s[64:65]
	s_add_u32 m0, s83, 0x2000
	s_nop 0
	global_load_lds_dwordx4 v12, s[64:65]
	s_add_u32 m0, s83, 0x3000
	s_nop 0
	global_load_lds_dwordx4 v13, s[64:65]
	s_add_u32 m0, s83, 0x4000
	s_nop 0
	global_load_lds_dwordx4 v14, s[64:65]
	s_add_u32 m0, s83, 0x5000
	s_nop 0
	global_load_lds_dwordx4 v20, s[66:67]
	s_add_u32 m0, s83, 0x6000
	s_nop 0
	global_load_lds_dwordx4 v21, s[66:67]
	s_add_u32 m0, s83, 0x7000
	s_nop 0
	global_load_lds_dwordx4 v22, s[66:67]
	s_add_u32 m0, s83, 0x8000
	s_nop 0
	global_load_lds_dwordx4 v23, s[66:67]
	s_add_u32 m0, s83, 0x9000
	s_nop 0
	global_load_lds_dwordx4 v24, s[66:67]
	s_add_u32 m0, s83, 0xa000
	s_nop 0
	global_load_lds_dwordx4 v25, s[66:67]
	s_add_u32 m0, s83, 0xb000
	s_nop 0
	global_load_lds_dwordx4 v26, s[66:67]
	s_add_u32 m0, s83, 0xc000
	s_nop 0
	global_load_lds_dwordx4 v27, s[66:67]
	s_add_u32 s64, s64, 0x80
	s_addc_u32 s65, s65, 0
	s_add_u32 s66, s66, 0x20000
	s_addc_u32 s67, s67, 0
	s_add_u32 s83, s70, s82
	s_add_u32 m0, s83, 0x0
	s_nop 0
	global_load_lds_dwordx4 v10, s[64:65]
	s_add_u32 m0, s83, 0x1000
	s_nop 0
	global_load_lds_dwordx4 v11, s[64:65]
	s_add_u32 m0, s83, 0x2000
	s_nop 0
	global_load_lds_dwordx4 v12, s[64:65]
	s_add_u32 m0, s83, 0x3000
	s_nop 0
	global_load_lds_dwordx4 v13, s[64:65]
	s_add_u32 m0, s83, 0x4000
	s_nop 0
	global_load_lds_dwordx4 v14, s[64:65]
	s_add_u32 m0, s83, 0x5000
	s_nop 0
	global_load_lds_dwordx4 v20, s[66:67]
	s_add_u32 m0, s83, 0x6000
	s_nop 0
	global_load_lds_dwordx4 v21, s[66:67]
	v_add_u32_e32 v34, s80, v30
	v_add_u32_e32 v35, s80, v31
	v_add_u32_e32 v36, s80, v32
	v_add_u32_e32 v37, s80, v33
	v_add_u32_e32 v48, s80, v40
	v_add_u32_e32 v49, s80, v41
	v_add_u32_e32 v50, s80, v42
	v_add_u32_e32 v51, s80, v43
	v_add_u32_e32 v52, s80, v44
	v_add_u32_e32 v53, s80, v45
	v_add_u32_e32 v54, s80, v46
	v_add_u32_e32 v55, s80, v47
	s_waitcnt vmcnt(20)
	s_barrier
	ds_read_b128 v[64:67], v34 offset:0
	ds_read_b128 v[68:71], v35 offset:2048
	ds_read_b128 v[72:75], v34 offset:4096
	ds_read_b128 v[76:79], v35 offset:6144
	ds_read_b128 v[80:83], v34 offset:8192
	ds_read_b64_tr_b16 v[100:101], v48 offset:0
	ds_read_b64_tr_b16 v[102:103], v48 offset:1024
	ds_read_b64_tr_b16 v[104:105], v49 offset:0
	ds_read_b64_tr_b16 v[106:107], v49 offset:1024
	ds_read_b64_tr_b16 v[108:109], v50 offset:0
	ds_read_b64_tr_b16 v[110:111], v50 offset:1024
	ds_read_b64_tr_b16 v[112:113], v51 offset:0
	ds_read_b64_tr_b16 v[114:115], v51 offset:1024
	ds_read_b64_tr_b16 v[116:117], v52 offset:0
	ds_read_b64_tr_b16 v[118:119], v52 offset:1024
	ds_read_b64_tr_b16 v[120:121], v53 offset:0
	ds_read_b64_tr_b16 v[122:123], v53 offset:1024
	ds_read_b64_tr_b16 v[124:125], v54 offset:0
	ds_read_b64_tr_b16 v[126:127], v54 offset:1024
	ds_read_b64_tr_b16 v[128:129], v55 offset:0
	ds_read_b64_tr_b16 v[130:131], v55 offset:1024
	s_mov_b32 s63, 29
	s_nop 0

amdhsa.kernels:
  - .agpr_count:     0
    .args:
      - .actual_access:  read_only
        .address_space:  global
        .offset:         0
        .size:           8
        .value_kind:     global_buffer
      - .address_space:  global
        .offset:         8
        .size:           8
        .value_kind:     global_buffer
      - .actual_access:  read_only
        .address_space:  global
        .offset:         16
        .size:           8
        .value_kind:     global_buffer
      - .address_space:  global
        .offset:         24
        .size:           8
        .value_kind:     global_buffer
      - .offset:         32
        .size:           4
        .value_kind:     by_value
      - .actual_access:  write_only
        .address_space:  global
        .offset:         40
        .size:           8
        .value_kind:     global_buffer
      - .offset:         48
        .size:           4
        .value_kind:     hidden_block_count_x
      - .offset:         52
        .size:           4
        .value_kind:     hidden_block_count_y
      - .offset:         56
        .size:           4
        .value_kind:     hidden_block_count_z
      - .offset:         60
        .size:           2
        .value_kind:     hidden_group_size_x
      - .offset:         62
        .size:           2
        .value_kind:     hidden_group_size_y
      - .offset:         64
        .size:           2
        .value_kind:     hidden_group_size_z
      - .offset:         66
        .size:           2
        .value_kind:     hidden_remainder_x
      - .offset:         68
        .size:           2
        .value_kind:     hidden_remainder_y
      - .offset:         70
        .size:           2
        .value_kind:     hidden_remainder_z
      - .offset:         88
        .size:           8
        .value_kind:     hidden_global_offset_x
      - .offset:         96
        .size:           8
        .value_kind:     hidden_global_offset_y
      - .offset:         104
        .size:           8
        .value_kind:     hidden_global_offset_z
      - .offset:         112
        .size:           2
        .value_kind:     hidden_grid_dims
    .group_segment_fixed_size: 0
    .kernarg_segment_align: 8
    .kernarg_segment_size: 304
    .language:       OpenCL C
    .language_version:
      - 2
      - 0
    .max_flat_workgroup_size: 256
    .name:           _Z5cvt_wPKfPDF16_S0_S1_iPi
    .private_segment_fixed_size: 0
    .sgpr_count:     30
    .sgpr_spill_count: 0
    .symbol:         _Z5cvt_wPKfPDF16_S0_S1_iPi.kd
    .uniform_work_group_size: 1
    .uses_dynamic_stack: false
    .vgpr_count:     40
    .vgpr_spill_count: 0
    .wavefront_size: 64
  - .agpr_count:     0
    .args:
      - .actual_access:  read_only
        .address_space:  global
        .offset:         0
        .size:           8
        .value_kind:     global_buffer
      - .actual_access:  read_only
        .address_space:  global
        .offset:         8
        .size:           8
        .value_kind:     global_buffer
      - .actual_access:  read_only
        .address_space:  global
        .offset:         16
        .size:           8
        .value_kind:     global_buffer
      - .actual_access:  write_only
        .address_space:  global
        .offset:         24
        .size:           8
        .value_kind:     global_buffer
      - .address_space:  global
        .offset:         32
        .size:           8
        .value_kind:     global_buffer
      - .actual_access:  write_only
        .address_space:  global
        .offset:         40
        .size:           8
        .value_kind:     global_buffer
      - .actual_access:  write_only
        .address_space:  global
        .offset:         48
        .size:           8
        .value_kind:     global_buffer
      - .actual_access:  read_only
        .address_space:  global
        .offset:         56
        .size:           8
        .value_kind:     global_buffer
      - .address_space:  global
        .offset:         64
        .size:           8
        .value_kind:     global_buffer
      - .offset:         72
        .size:           4
        .value_kind:     by_value
      - .offset:         80
        .size:           4
        .value_kind:     hidden_block_count_x
      - .offset:         84
        .size:           4
        .value_kind:     hidden_block_count_y
      - .offset:         88
        .size:           4
        .value_kind:     hidden_block_count_z
      - .offset:         92
        .size:           2
        .value_kind:     hidden_group_size_x
      - .offset:         94
        .size:           2
        .value_kind:     hidden_group_size_y
      - .offset:         96
        .size:           2
        .value_kind:     hidden_group_size_z
      - .offset:         98
        .size:           2
        .value_kind:     hidden_remainder_x
      - .offset:         100
        .size:           2
        .value_kind:     hidden_remainder_y
      - .offset:         102
        .size:           2
        .value_kind:     hidden_remainder_z
      - .offset:         120
        .size:           8
        .value_kind:     hidden_global_offset_x
      - .offset:         128
        .size:           8
        .value_kind:     hidden_global_offset_y
      - .offset:         136
        .size:           8
        .value_kind:     hidden_global_offset_z
      - .offset:         144
        .size:           2
        .value_kind:     hidden_grid_dims
    .group_segment_fixed_size: 32928
    .kernarg_segment_align: 8
    .kernarg_segment_size: 336
    .language:       OpenCL C
    .language_version:
      - 2
      - 0
    .max_flat_workgroup_size: 512
    .name:           _Z11gate_kernelPKfS0_S0_PDF16_PiS2_PfS0_S1_i
    .private_segment_fixed_size: 0
    .sgpr_count:     66
    .sgpr_spill_count: 0
    .symbol:         _Z11gate_kernelPKfS0_S0_PDF16_PiS2_PfS0_S1_i.kd
    .uniform_work_group_size: 1
    .uses_dynamic_stack: false
    .vgpr_count:     115
    .vgpr_spill_count: 0
    .wavefront_size: 64
  - .agpr_count:     0
    .args:
      - .address_space:  global
        .offset:         0
        .size:           8
        .value_kind:     global_buffer
      - .address_space:  global
        .offset:         8
        .size:           8
        .value_kind:     global_buffer
      - .actual_access:  read_only
        .address_space:  global
        .offset:         16
        .size:           8
        .value_kind:     global_buffer
      - .address_space:  global
        .offset:         24
        .size:           8
        .value_kind:     global_buffer
      - .actual_access:  read_only
        .address_space:  global
        .offset:         32
        .size:           8
        .value_kind:     global_buffer
      - .actual_access:  read_only
        .address_space:  global
        .offset:         40
        .size:           8
        .value_kind:     global_buffer
      - .actual_access:  read_only
        .address_space:  global
        .offset:         48
        .size:           8
        .value_kind:     global_buffer
      - .offset:         56
        .size:           4
        .value_kind:     hidden_block_count_x
      - .offset:         60
        .size:           4
        .value_kind:     hidden_block_count_y
      - .offset:         64
        .size:           4
        .value_kind:     hidden_block_count_z
      - .offset:         68
        .size:           2
        .value_kind:     hidden_group_size_x
      - .offset:         70
        .size:           2
        .value_kind:     hidden_group_size_y
      - .offset:         72
        .size:           2
        .value_kind:     hidden_group_size_z
      - .offset:         74
        .size:           2
        .value_kind:     hidden_remainder_x
      - .offset:         76
        .size:           2
        .value_kind:     hidden_remainder_y
      - .offset:         78
        .size:           2
        .value_kind:     hidden_remainder_z
      - .offset:         96
        .size:           8
        .value_kind:     hidden_global_offset_x
      - .offset:         104
        .size:           8
        .value_kind:     hidden_global_offset_y
      - .offset:         112
        .size:           8
        .value_kind:     hidden_global_offset_z
      - .offset:         120
        .size:           2
        .value_kind:     hidden_grid_dims
      - .offset:         176
        .size:           4
        .value_kind:     hidden_dynamic_lds_size
    .group_segment_fixed_size: 0
    .kernarg_segment_align: 8
    .kernarg_segment_size: 312
    .language:       OpenCL C
    .language_version:
      - 2
      - 0
    .max_flat_workgroup_size: 256
    .name:           _Z8moe_gemmILi1024ELi2048ELb1EEvPKDF16_S1_PKfPDF16_PfPKiS7_
    .private_segment_fixed_size: 0
    .sgpr_count:     93
    .sgpr_spill_count: 0
    .symbol:         _Z8moe_gemmILi1024ELi2048ELb1EEvPKDF16_S1_PKfPDF16_PfPKiS7_.kd
    .uniform_work_group_size: 1
    .uses_dynamic_stack: false
    .vgpr_count:     206
    .vgpr_spill_count: 0
    .wavefront_size: 64
  - .agpr_count:     256
    .args:
      - .address_space:  global
        .offset:         0
        .size:           8
        .value_kind:     global_buffer
      - .address_space:  global
        .offset:         8
        .size:           8
        .value_kind:     global_buffer
      - .actual_access:  read_only
        .address_space:  global
        .offset:         16
        .size:           8
        .value_kind:     global_buffer
      - .actual_access:  read_only
        .address_space:  global
        .offset:         24
        .size:           8
        .value_kind:     global_buffer
      - .address_space:  global
        .offset:         32
        .size:           8
        .value_kind:     global_buffer
      - .actual_access:  read_only
        .address_space:  global
        .offset:         40
        .size:           8
        .value_kind:     global_buffer
      - .actual_access:  read_only
        .address_space:  global
        .offset:         48
        .size:           8
        .value_kind:     global_buffer
      - .offset:         56
        .size:           4
        .value_kind:     hidden_block_count_x
      - .offset:         60
        .size:           4
        .value_kind:     hidden_block_count_y
      - .offset:         64
        .size:           4
        .value_kind:     hidden_block_count_z
      - .offset:         68
        .size:           2
        .value_kind:     hidden_group_size_x
      - .offset:         70
        .size:           2
        .value_kind:     hidden_group_size_y
      - .offset:         72
        .size:           2
        .value_kind:     hidden_group_size_z
      - .offset:         74
        .size:           2
        .value_kind:     hidden_remainder_x
      - .offset:         76
        .size:           2
        .value_kind:     hidden_remainder_y
      - .offset:         78
        .size:           2
        .value_kind:     hidden_remainder_z
      - .offset:         96
        .size:           8
        .value_kind:     hidden_global_offset_x
      - .offset:         104
        .size:           8
        .value_kind:     hidden_global_offset_y
      - .offset:         112
        .size:           8
        .value_kind:     hidden_global_offset_z
      - .offset:         120
        .size:           2
        .value_kind:     hidden_grid_dims
      - .offset:         176
        .size:           4
        .value_kind:     hidden_dynamic_lds_size
    .group_segment_fixed_size: 86016
    .kernarg_segment_align: 8
    .kernarg_segment_size: 312
    .language:       OpenCL C
    .language_version:
      - 2
      - 0
    .max_flat_workgroup_size: 256
    .name:           _Z8moe_gemmILi2048ELi1024ELb0EEvPKDF16_S1_PKfPDF16_PfPKiS7_
    .private_segment_fixed_size: 0
    .sgpr_count:     96
    .sgpr_spill_count: 0
    .symbol:         _Z8moe_gemmILi2048ELi1024ELb0EEvPKDF16_S1_PKfPDF16_PfPKiS7_.kd
    .uniform_work_group_size: 1
    .uses_dynamic_stack: false
    .vgpr_count:     512
    .vgpr_spill_count: 0
    .wavefront_size: 64
